# in-proj rope epilogue: rope cos/sin loads of the next row block issued before the current block's maths, counted waits
# speedup vs baseline: 1.0125x; 1.0125x over previous
.LBB0_140:
	s_or_b64 exec, exec, s[30:31]
	s_xor_b64 s[30:31], s[34:35], -1
	s_and_saveexec_b64 s[34:35], s[30:31]
	s_xor_b64 s[34:35], exec, s[34:35]
	s_or_saveexec_b64 s[34:35], s[34:35]
	s_lshl_b32 s33, s88, 8
	s_add_i32 s33, s33, s58
	v_add_u32_e32 v158, s33, v152
	v_lshrrev_b32_e32 v150, 1, v153
	v_and_b32_e32 v150, 28, v150
	v_lshlrev_b32_e32 v151, 7, v158
	v_and_b32_e32 v152, 0xfff80, v151
	v_lshlrev_b32_e32 v150, 2, v150
	s_xor_b64 exec, exec, s[34:35]
	s_cbranch_execz .LBB0_142
	v_mov_b32_e32 v200, v158
	v_lshlrev_b32_e32 v200, 7, v200
	v_and_b32_e32 v200, 0xfff80, v200
	v_mov_b32_e32 v201, v141
	v_mov_b32_e32 v151, v141
	v_lshl_add_u64 v[196:197], s[10:11], 0, v[200:201]
	v_lshl_add_u64 v[198:199], s[12:13], 0, v[200:201]
	v_lshl_add_u64 v[196:197], v[196:197], 0, v[150:151]
	v_lshl_add_u64 v[198:199], v[198:199], 0, v[150:151]
	global_load_dwordx4 v[180:183], v[196:197], off
	global_load_dwordx4 v[184:187], v[198:199], off
	v_add_u32_e32 v200, 0x10, v158
	v_lshlrev_b32_e32 v200, 7, v200
	v_and_b32_e32 v200, 0xfff80, v200
	v_mov_b32_e32 v201, v141
	v_mov_b32_e32 v151, v141
	v_lshl_add_u64 v[196:197], s[10:11], 0, v[200:201]
	v_lshl_add_u64 v[198:199], s[12:13], 0, v[200:201]
	v_lshl_add_u64 v[196:197], v[196:197], 0, v[150:151]
	v_lshl_add_u64 v[198:199], v[198:199], 0, v[150:151]
	global_load_dwordx4 v[188:191], v[196:197], off
	global_load_dwordx4 v[192:195], v[198:199], off
	s_waitcnt vmcnt(2)
	v_pk_mul_f32 v[176:177], v[122:123], v[184:185] op_sel:[1,0] op_sel_hi:[0,0]
	v_pk_mul_f32 v[184:185], v[124:125], v[184:185] op_sel:[1,1] op_sel_hi:[0,1]
	v_pk_fma_f32 v[178:179], v[122:123], v[180:181], v[176:177] neg_lo:[0,0,1] neg_hi:[0,0,1]
	v_pk_fma_f32 v[122:123], v[122:123], v[180:181], v[176:177] op_sel_hi:[1,0,1]
	v_pk_fma_f32 v[176:177], v[124:125], v[180:181], v[184:185] op_sel:[0,1,0] neg_lo:[0,0,1] neg_hi:[0,0,1]
	v_pk_fma_f32 v[124:125], v[124:125], v[180:181], v[184:185] op_sel:[0,1,0]
	v_pk_mul_f32 v[180:181], v[126:127], v[186:187] op_sel:[1,0] op_sel_hi:[0,0]
	v_pk_fma_f32 v[184:185], v[126:127], v[182:183], v[180:181] neg_lo:[0,0,1] neg_hi:[0,0,1]
	v_pk_fma_f32 v[126:127], v[126:127], v[182:183], v[180:181] op_sel_hi:[1,0,1]
	v_mov_b32_e32 v182, v187
	v_mov_b32_e32 v185, v127
	v_mov_b32_e32 v180, v183
	v_pk_mul_f32 v[182:183], v[128:129], v[182:183] op_sel:[1,0] op_sel_hi:[0,0]
	v_pk_mul_f32 v[126:127], v[156:157], v[184:185] op_sel_hi:[0,1]
	v_pk_fma_f32 v[184:185], v[128:129], v[180:181], v[182:183] op_sel_hi:[1,0,1] neg_lo:[0,0,1] neg_hi:[0,0,1]
	v_pk_fma_f32 v[128:129], v[128:129], v[180:181], v[182:183] op_sel_hi:[1,0,1]
	v_mov_b32_e32 v179, v123
	v_mov_b32_e32 v177, v125
	v_mov_b32_e32 v185, v129
	v_pk_mul_f32 v[122:123], v[156:157], v[178:179] op_sel_hi:[0,1]
	v_pk_mul_f32 v[124:125], v[156:157], v[176:177] op_sel_hi:[0,1]
	v_pk_mul_f32 v[128:129], v[156:157], v[184:185] op_sel_hi:[0,1]
.LBB0_142:
	s_or_b64 exec, exec, s[34:35]
	v_ashrrev_i32_e32 v159, 31, v158
	v_cvt_pk_bf16_f32 v169, v124, v125
	v_lshlrev_b64 v[124:125], 7, v[158:159]
	v_cvt_pk_bf16_f32 v168, v122, v123
	v_cvt_pk_bf16_f32 v170, v126, v127
	v_cvt_pk_bf16_f32 v171, v128, v129
	v_lshl_add_u64 v[122:123], v[154:155], 0, v[124:125]
	global_store_dwordx4 v[122:123], v[168:171], off
	s_and_saveexec_b64 s[34:35], s[30:31]
	s_xor_b64 s[34:35], exec, s[34:35]
	s_or_saveexec_b64 s[34:35], s[34:35]
	v_add_u32_e32 v126, 16, v158
	v_lshlrev_b32_e32 v122, 7, v126
	v_and_b32_e32 v122, 0xfff80, v122
	s_xor_b64 exec, exec, s[34:35]
	s_cbranch_execz .LBB0_144
	v_add_u32_e32 v200, 0x20, v158
	v_lshlrev_b32_e32 v200, 7, v200
	v_and_b32_e32 v200, 0xfff80, v200
	v_mov_b32_e32 v201, v141
	v_mov_b32_e32 v151, v141
	v_lshl_add_u64 v[196:197], s[10:11], 0, v[200:201]
	v_lshl_add_u64 v[198:199], s[12:13], 0, v[200:201]
	v_lshl_add_u64 v[196:197], v[196:197], 0, v[150:151]
	v_lshl_add_u64 v[198:199], v[198:199], 0, v[150:151]
	global_load_dwordx4 v[180:183], v[196:197], off
	global_load_dwordx4 v[184:187], v[198:199], off
	s_waitcnt vmcnt(3)
	v_pk_mul_f32 v[128:129], v[118:119], v[192:193] op_sel:[1,0] op_sel_hi:[0,0]
	v_pk_fma_f32 v[176:177], v[118:119], v[188:189], v[128:129] neg_lo:[0,0,1] neg_hi:[0,0,1]
	v_pk_fma_f32 v[118:119], v[118:119], v[188:189], v[128:129] op_sel_hi:[1,0,1]
	v_pk_mul_f32 v[128:129], v[120:121], v[192:193] op_sel:[1,1] op_sel_hi:[0,1]
	v_pk_fma_f32 v[192:193], v[120:121], v[188:189], v[128:129] op_sel:[0,1,0] neg_lo:[0,0,1] neg_hi:[0,0,1]
	v_pk_fma_f32 v[120:121], v[120:121], v[188:189], v[128:129] op_sel:[0,1,0]
	v_pk_mul_f32 v[128:129], v[114:115], v[194:195] op_sel:[1,0] op_sel_hi:[0,0]
	v_pk_fma_f32 v[188:189], v[114:115], v[190:191], v[128:129] neg_lo:[0,0,1] neg_hi:[0,0,1]
	v_pk_fma_f32 v[114:115], v[114:115], v[190:191], v[128:129] op_sel_hi:[1,0,1]
	v_mov_b32_e32 v128, v191
	v_mov_b32_e32 v189, v115
	v_pk_mul_f32 v[114:115], v[156:157], v[188:189] op_sel_hi:[0,1]
	v_mov_b32_e32 v188, v195
	v_pk_mul_f32 v[188:189], v[116:117], v[188:189] op_sel:[1,0] op_sel_hi:[0,0]
	v_pk_fma_f32 v[190:191], v[116:117], v[128:129], v[188:189] op_sel_hi:[1,0,1] neg_lo:[0,0,1] neg_hi:[0,0,1]
	v_pk_fma_f32 v[116:117], v[116:117], v[128:129], v[188:189] op_sel_hi:[1,0,1]
	v_mov_b32_e32 v177, v119
	v_mov_b32_e32 v193, v121
	v_mov_b32_e32 v191, v117
	v_pk_mul_f32 v[118:119], v[156:157], v[176:177] op_sel_hi:[0,1]
	v_pk_mul_f32 v[120:121], v[156:157], v[192:193] op_sel_hi:[0,1]
	v_pk_mul_f32 v[116:117], v[156:157], v[190:191] op_sel_hi:[0,1]
.LBB0_144:
	s_or_b64 exec, exec, s[34:35]
	v_ashrrev_i32_e32 v127, 31, v126
	v_cvt_pk_bf16_f32 v118, v118, v119
	v_cvt_pk_bf16_f32 v119, v120, v121
	v_cvt_pk_bf16_f32 v121, v116, v117
	v_lshlrev_b64 v[116:117], 7, v[126:127]
	v_cvt_pk_bf16_f32 v120, v114, v115
	v_lshl_add_u64 v[114:115], v[154:155], 0, v[116:117]
	global_store_dwordx4 v[114:115], v[118:121], off
	s_and_saveexec_b64 s[34:35], s[30:31]
	s_xor_b64 s[34:35], exec, s[34:35]
	s_or_saveexec_b64 s[34:35], s[34:35]
	v_add_u32_e32 v118, 32, v158
	v_lshlrev_b32_e32 v114, 7, v118
	v_and_b32_e32 v114, 0xfff80, v114
	s_xor_b64 exec, exec, s[34:35]
	s_cbranch_execz .LBB0_146
	v_add_u32_e32 v200, 0x30, v158
	v_lshlrev_b32_e32 v200, 7, v200
	v_and_b32_e32 v200, 0xfff80, v200
	v_mov_b32_e32 v201, v141
	v_mov_b32_e32 v151, v141
	v_lshl_add_u64 v[196:197], s[10:11], 0, v[200:201]
	v_lshl_add_u64 v[198:199], s[12:13], 0, v[200:201]
	v_lshl_add_u64 v[196:197], v[196:197], 0, v[150:151]
	v_lshl_add_u64 v[198:199], v[198:199], 0, v[150:151]
	global_load_dwordx4 v[188:191], v[196:197], off
	global_load_dwordx4 v[192:195], v[198:199], off
	s_waitcnt vmcnt(3)
	v_pk_mul_f32 v[120:121], v[110:111], v[184:185] op_sel:[1,0] op_sel_hi:[0,0]
	v_pk_fma_f32 v[172:173], v[110:111], v[180:181], v[120:121] neg_lo:[0,0,1] neg_hi:[0,0,1]
	v_pk_fma_f32 v[110:111], v[110:111], v[180:181], v[120:121] op_sel_hi:[1,0,1]
	v_pk_mul_f32 v[120:121], v[112:113], v[184:185] op_sel:[1,1] op_sel_hi:[0,1]
	v_pk_fma_f32 v[184:185], v[112:113], v[180:181], v[120:121] op_sel:[0,1,0] neg_lo:[0,0,1] neg_hi:[0,0,1]
	v_pk_fma_f32 v[112:113], v[112:113], v[180:181], v[120:121] op_sel:[0,1,0]
	v_pk_mul_f32 v[120:121], v[106:107], v[186:187] op_sel:[1,0] op_sel_hi:[0,0]
	v_pk_fma_f32 v[180:181], v[106:107], v[182:183], v[120:121] neg_lo:[0,0,1] neg_hi:[0,0,1]
	v_pk_fma_f32 v[106:107], v[106:107], v[182:183], v[120:121] op_sel_hi:[1,0,1]
	v_mov_b32_e32 v120, v183
	v_mov_b32_e32 v181, v107
	v_pk_mul_f32 v[106:107], v[156:157], v[180:181] op_sel_hi:[0,1]
	v_mov_b32_e32 v180, v187
	v_pk_mul_f32 v[180:181], v[108:109], v[180:181] op_sel:[1,0] op_sel_hi:[0,0]
	v_pk_fma_f32 v[182:183], v[108:109], v[120:121], v[180:181] op_sel_hi:[1,0,1] neg_lo:[0,0,1] neg_hi:[0,0,1]
	v_pk_fma_f32 v[108:109], v[108:109], v[120:121], v[180:181] op_sel_hi:[1,0,1]
	v_mov_b32_e32 v173, v111
	v_mov_b32_e32 v185, v113
	v_mov_b32_e32 v183, v109
	v_pk_mul_f32 v[110:111], v[156:157], v[172:173] op_sel_hi:[0,1]
	v_pk_mul_f32 v[112:113], v[156:157], v[184:185] op_sel_hi:[0,1]
	v_pk_mul_f32 v[108:109], v[156:157], v[182:183] op_sel_hi:[0,1]
.LBB0_146:
	s_or_b64 exec, exec, s[34:35]
	v_ashrrev_i32_e32 v119, 31, v118
	v_cvt_pk_bf16_f32 v110, v110, v111
	v_cvt_pk_bf16_f32 v111, v112, v113
	v_cvt_pk_bf16_f32 v113, v108, v109
	v_lshlrev_b64 v[108:109], 7, v[118:119]
	v_cvt_pk_bf16_f32 v112, v106, v107
	v_lshl_add_u64 v[106:107], v[154:155], 0, v[108:109]
	global_store_dwordx4 v[106:107], v[110:113], off
	s_and_saveexec_b64 s[34:35], s[30:31]
	s_xor_b64 s[34:35], exec, s[34:35]
	s_or_saveexec_b64 s[34:35], s[34:35]
	v_add_u32_e32 v110, 48, v158
	v_lshlrev_b32_e32 v106, 7, v110
	v_and_b32_e32 v106, 0xfff80, v106
	s_xor_b64 exec, exec, s[34:35]
	s_cbranch_execz .LBB0_148
	v_add_u32_e32 v200, 0x80, v158
	v_lshlrev_b32_e32 v200, 7, v200
	v_and_b32_e32 v200, 0xfff80, v200
	v_mov_b32_e32 v201, v141
	v_mov_b32_e32 v151, v141
	v_lshl_add_u64 v[196:197], s[10:11], 0, v[200:201]
	v_lshl_add_u64 v[198:199], s[12:13], 0, v[200:201]
	v_lshl_add_u64 v[196:197], v[196:197], 0, v[150:151]
	v_lshl_add_u64 v[198:199], v[198:199], 0, v[150:151]
	global_load_dwordx4 v[180:183], v[196:197], off
	global_load_dwordx4 v[184:187], v[198:199], off
	s_waitcnt vmcnt(3)
	v_pk_mul_f32 v[112:113], v[102:103], v[192:193] op_sel:[1,0] op_sel_hi:[0,0]
	v_pk_fma_f32 v[168:169], v[102:103], v[188:189], v[112:113] neg_lo:[0,0,1] neg_hi:[0,0,1]
	v_pk_fma_f32 v[102:103], v[102:103], v[188:189], v[112:113] op_sel_hi:[1,0,1]
	v_pk_mul_f32 v[112:113], v[104:105], v[192:193] op_sel:[1,1] op_sel_hi:[0,1]
	v_pk_fma_f32 v[192:193], v[104:105], v[188:189], v[112:113] op_sel:[0,1,0] neg_lo:[0,0,1] neg_hi:[0,0,1]
	v_pk_fma_f32 v[104:105], v[104:105], v[188:189], v[112:113] op_sel:[0,1,0]
	v_pk_mul_f32 v[112:113], v[98:99], v[194:195] op_sel:[1,0] op_sel_hi:[0,0]
	v_pk_fma_f32 v[188:189], v[98:99], v[190:191], v[112:113] neg_lo:[0,0,1] neg_hi:[0,0,1]
	v_pk_fma_f32 v[98:99], v[98:99], v[190:191], v[112:113] op_sel_hi:[1,0,1]
	v_mov_b32_e32 v112, v191
	v_mov_b32_e32 v189, v99
	v_pk_mul_f32 v[98:99], v[156:157], v[188:189] op_sel_hi:[0,1]
	v_mov_b32_e32 v188, v195
	v_pk_mul_f32 v[188:189], v[100:101], v[188:189] op_sel:[1,0] op_sel_hi:[0,0]
	v_pk_fma_f32 v[190:191], v[100:101], v[112:113], v[188:189] op_sel_hi:[1,0,1] neg_lo:[0,0,1] neg_hi:[0,0,1]
	v_pk_fma_f32 v[100:101], v[100:101], v[112:113], v[188:189] op_sel_hi:[1,0,1]
	v_mov_b32_e32 v169, v103
	v_mov_b32_e32 v193, v105
	v_mov_b32_e32 v191, v101
	v_pk_mul_f32 v[102:103], v[156:157], v[168:169] op_sel_hi:[0,1]
	v_pk_mul_f32 v[104:105], v[156:157], v[192:193] op_sel_hi:[0,1]
	v_pk_mul_f32 v[100:101], v[156:157], v[190:191] op_sel_hi:[0,1]
.LBB0_148:
	s_or_b64 exec, exec, s[34:35]
	v_ashrrev_i32_e32 v111, 31, v110
	v_cvt_pk_bf16_f32 v102, v102, v103
	v_cvt_pk_bf16_f32 v103, v104, v105
	v_cvt_pk_bf16_f32 v105, v100, v101
	v_lshlrev_b64 v[100:101], 7, v[110:111]
	v_cvt_pk_bf16_f32 v104, v98, v99
	v_lshl_add_u64 v[98:99], v[154:155], 0, v[100:101]
	global_store_dwordx4 v[98:99], v[102:105], off
	s_and_saveexec_b64 s[34:35], s[30:31]
	s_xor_b64 s[34:35], exec, s[34:35]
	s_or_saveexec_b64 s[34:35], s[34:35]
	v_add_u32_e32 v102, 0x80, v158
	v_lshlrev_b32_e32 v98, 7, v102
	v_and_b32_e32 v98, 0xfff80, v98
	s_xor_b64 exec, exec, s[34:35]
	s_cbranch_execz .LBB0_150
	v_add_u32_e32 v200, 0x90, v158
	v_lshlrev_b32_e32 v200, 7, v200
	v_and_b32_e32 v200, 0xfff80, v200
	v_mov_b32_e32 v201, v141
	v_mov_b32_e32 v151, v141
	v_lshl_add_u64 v[196:197], s[10:11], 0, v[200:201]
	v_lshl_add_u64 v[198:199], s[12:13], 0, v[200:201]
	v_lshl_add_u64 v[196:197], v[196:197], 0, v[150:151]
	v_lshl_add_u64 v[198:199], v[198:199], 0, v[150:151]
	global_load_dwordx4 v[188:191], v[196:197], off
	global_load_dwordx4 v[192:195], v[198:199], off
	s_waitcnt vmcnt(3)
	v_pk_mul_f32 v[104:105], v[94:95], v[184:185] op_sel:[1,0] op_sel_hi:[0,0]
	v_pk_fma_f32 v[126:127], v[94:95], v[180:181], v[104:105] neg_lo:[0,0,1] neg_hi:[0,0,1]
	v_pk_fma_f32 v[94:95], v[94:95], v[180:181], v[104:105] op_sel_hi:[1,0,1]
	v_pk_mul_f32 v[104:105], v[96:97], v[184:185] op_sel:[1,1] op_sel_hi:[0,1]
	v_pk_fma_f32 v[184:185], v[96:97], v[180:181], v[104:105] op_sel:[0,1,0] neg_lo:[0,0,1] neg_hi:[0,0,1]
	v_pk_fma_f32 v[96:97], v[96:97], v[180:181], v[104:105] op_sel:[0,1,0]
	v_pk_mul_f32 v[104:105], v[90:91], v[186:187] op_sel:[1,0] op_sel_hi:[0,0]
	v_pk_fma_f32 v[180:181], v[90:91], v[182:183], v[104:105] neg_lo:[0,0,1] neg_hi:[0,0,1]
	v_pk_fma_f32 v[90:91], v[90:91], v[182:183], v[104:105] op_sel_hi:[1,0,1]
	v_mov_b32_e32 v104, v183
	v_mov_b32_e32 v181, v91
	v_pk_mul_f32 v[90:91], v[156:157], v[180:181] op_sel_hi:[0,1]
	v_mov_b32_e32 v180, v187
	v_pk_mul_f32 v[180:181], v[92:93], v[180:181] op_sel:[1,0] op_sel_hi:[0,0]
	v_pk_fma_f32 v[182:183], v[92:93], v[104:105], v[180:181] op_sel_hi:[1,0,1] neg_lo:[0,0,1] neg_hi:[0,0,1]
	v_pk_fma_f32 v[92:93], v[92:93], v[104:105], v[180:181] op_sel_hi:[1,0,1]
	v_mov_b32_e32 v127, v95
	v_mov_b32_e32 v185, v97
	v_mov_b32_e32 v183, v93
	v_pk_mul_f32 v[94:95], v[156:157], v[126:127] op_sel_hi:[0,1]
	v_pk_mul_f32 v[96:97], v[156:157], v[184:185] op_sel_hi:[0,1]
	v_pk_mul_f32 v[92:93], v[156:157], v[182:183] op_sel_hi:[0,1]
.LBB0_150:
	s_or_b64 exec, exec, s[34:35]
	v_ashrrev_i32_e32 v103, 31, v102
	v_cvt_pk_bf16_f32 v94, v94, v95
	v_cvt_pk_bf16_f32 v95, v96, v97
	v_cvt_pk_bf16_f32 v97, v92, v93
	v_lshlrev_b64 v[92:93], 7, v[102:103]
	v_cvt_pk_bf16_f32 v96, v90, v91
	v_lshl_add_u64 v[90:91], v[154:155], 0, v[92:93]
	global_store_dwordx4 v[90:91], v[94:97], off
	s_and_saveexec_b64 s[34:35], s[30:31]
	s_xor_b64 s[34:35], exec, s[34:35]
	s_or_saveexec_b64 s[34:35], s[34:35]
	v_add_u32_e32 v94, 0x90, v158
	v_lshlrev_b32_e32 v90, 7, v94
	v_and_b32_e32 v90, 0xfff80, v90
	s_xor_b64 exec, exec, s[34:35]
	s_cbranch_execz .LBB0_152
	v_add_u32_e32 v200, 0xa0, v158
	v_lshlrev_b32_e32 v200, 7, v200
	v_and_b32_e32 v200, 0xfff80, v200
	v_mov_b32_e32 v201, v141
	v_mov_b32_e32 v151, v141
	v_lshl_add_u64 v[196:197], s[10:11], 0, v[200:201]
	v_lshl_add_u64 v[198:199], s[12:13], 0, v[200:201]
	v_lshl_add_u64 v[196:197], v[196:197], 0, v[150:151]
	v_lshl_add_u64 v[198:199], v[198:199], 0, v[150:151]
	global_load_dwordx4 v[180:183], v[196:197], off
	global_load_dwordx4 v[184:187], v[198:199], off
	s_waitcnt vmcnt(3)
	v_pk_mul_f32 v[96:97], v[86:87], v[192:193] op_sel:[1,0] op_sel_hi:[0,0]
	v_pk_fma_f32 v[118:119], v[86:87], v[188:189], v[96:97] neg_lo:[0,0,1] neg_hi:[0,0,1]
	v_pk_fma_f32 v[86:87], v[86:87], v[188:189], v[96:97] op_sel_hi:[1,0,1]
	v_pk_mul_f32 v[96:97], v[88:89], v[192:193] op_sel:[1,1] op_sel_hi:[0,1]
	v_pk_fma_f32 v[192:193], v[88:89], v[188:189], v[96:97] op_sel:[0,1,0] neg_lo:[0,0,1] neg_hi:[0,0,1]
	v_pk_fma_f32 v[88:89], v[88:89], v[188:189], v[96:97] op_sel:[0,1,0]
	v_pk_mul_f32 v[96:97], v[82:83], v[194:195] op_sel:[1,0] op_sel_hi:[0,0]
	v_pk_fma_f32 v[188:189], v[82:83], v[190:191], v[96:97] neg_lo:[0,0,1] neg_hi:[0,0,1]
	v_pk_fma_f32 v[82:83], v[82:83], v[190:191], v[96:97] op_sel_hi:[1,0,1]
	v_mov_b32_e32 v96, v191
	v_mov_b32_e32 v189, v83
	v_pk_mul_f32 v[82:83], v[156:157], v[188:189] op_sel_hi:[0,1]
	v_mov_b32_e32 v188, v195
	v_pk_mul_f32 v[188:189], v[84:85], v[188:189] op_sel:[1,0] op_sel_hi:[0,0]
	v_pk_fma_f32 v[190:191], v[84:85], v[96:97], v[188:189] op_sel_hi:[1,0,1] neg_lo:[0,0,1] neg_hi:[0,0,1]
	v_pk_fma_f32 v[84:85], v[84:85], v[96:97], v[188:189] op_sel_hi:[1,0,1]
	v_mov_b32_e32 v119, v87
	v_mov_b32_e32 v193, v89
	v_mov_b32_e32 v191, v85
	v_pk_mul_f32 v[86:87], v[156:157], v[118:119] op_sel_hi:[0,1]
	v_pk_mul_f32 v[88:89], v[156:157], v[192:193] op_sel_hi:[0,1]
	v_pk_mul_f32 v[84:85], v[156:157], v[190:191] op_sel_hi:[0,1]
.LBB0_152:
	s_or_b64 exec, exec, s[34:35]
	v_ashrrev_i32_e32 v95, 31, v94
	v_cvt_pk_bf16_f32 v86, v86, v87
	v_cvt_pk_bf16_f32 v87, v88, v89
	v_cvt_pk_bf16_f32 v89, v84, v85
	v_lshlrev_b64 v[84:85], 7, v[94:95]
	v_cvt_pk_bf16_f32 v88, v82, v83
	v_lshl_add_u64 v[82:83], v[154:155], 0, v[84:85]
	global_store_dwordx4 v[82:83], v[86:89], off
	s_and_saveexec_b64 s[34:35], s[30:31]
	s_xor_b64 s[34:35], exec, s[34:35]
	s_or_saveexec_b64 s[34:35], s[34:35]
	v_add_u32_e32 v86, 0xa0, v158
	v_lshlrev_b32_e32 v82, 7, v86
	v_and_b32_e32 v82, 0xfff80, v82
	s_xor_b64 exec, exec, s[34:35]
	s_cbranch_execz .LBB0_154
	v_add_u32_e32 v200, 0xb0, v158
	v_lshlrev_b32_e32 v200, 7, v200
	v_and_b32_e32 v200, 0xfff80, v200
	v_mov_b32_e32 v201, v141
	v_mov_b32_e32 v151, v141
	v_lshl_add_u64 v[196:197], s[10:11], 0, v[200:201]
	v_lshl_add_u64 v[198:199], s[12:13], 0, v[200:201]
	v_lshl_add_u64 v[196:197], v[196:197], 0, v[150:151]
	v_lshl_add_u64 v[198:199], v[198:199], 0, v[150:151]
	global_load_dwordx4 v[188:191], v[196:197], off
	global_load_dwordx4 v[192:195], v[198:199], off
	s_waitcnt vmcnt(3)
	v_pk_mul_f32 v[88:89], v[78:79], v[184:185] op_sel:[1,0] op_sel_hi:[0,0]
	v_pk_fma_f32 v[110:111], v[78:79], v[180:181], v[88:89] neg_lo:[0,0,1] neg_hi:[0,0,1]
	v_pk_fma_f32 v[78:79], v[78:79], v[180:181], v[88:89] op_sel_hi:[1,0,1]
	v_pk_mul_f32 v[88:89], v[80:81], v[184:185] op_sel:[1,1] op_sel_hi:[0,1]
	v_pk_fma_f32 v[184:185], v[80:81], v[180:181], v[88:89] op_sel:[0,1,0] neg_lo:[0,0,1] neg_hi:[0,0,1]
	v_pk_fma_f32 v[80:81], v[80:81], v[180:181], v[88:89] op_sel:[0,1,0]
	v_pk_mul_f32 v[88:89], v[74:75], v[186:187] op_sel:[1,0] op_sel_hi:[0,0]
	v_pk_fma_f32 v[180:181], v[74:75], v[182:183], v[88:89] neg_lo:[0,0,1] neg_hi:[0,0,1]
	v_pk_fma_f32 v[74:75], v[74:75], v[182:183], v[88:89] op_sel_hi:[1,0,1]
	v_mov_b32_e32 v88, v183
	v_mov_b32_e32 v181, v75
	v_pk_mul_f32 v[74:75], v[156:157], v[180:181] op_sel_hi:[0,1]
	v_mov_b32_e32 v180, v187
	v_pk_mul_f32 v[180:181], v[76:77], v[180:181] op_sel:[1,0] op_sel_hi:[0,0]
	v_pk_fma_f32 v[182:183], v[76:77], v[88:89], v[180:181] op_sel_hi:[1,0,1] neg_lo:[0,0,1] neg_hi:[0,0,1]
	v_pk_fma_f32 v[76:77], v[76:77], v[88:89], v[180:181] op_sel_hi:[1,0,1]
	v_mov_b32_e32 v111, v79
	v_mov_b32_e32 v185, v81
	v_mov_b32_e32 v183, v77
	v_pk_mul_f32 v[78:79], v[156:157], v[110:111] op_sel_hi:[0,1]
	v_pk_mul_f32 v[80:81], v[156:157], v[184:185] op_sel_hi:[0,1]
	v_pk_mul_f32 v[76:77], v[156:157], v[182:183] op_sel_hi:[0,1]
.LBB0_154:
	s_or_b64 exec, exec, s[34:35]
	v_ashrrev_i32_e32 v87, 31, v86
	v_cvt_pk_bf16_f32 v78, v78, v79
	v_cvt_pk_bf16_f32 v79, v80, v81
	v_cvt_pk_bf16_f32 v81, v76, v77
	v_lshlrev_b64 v[76:77], 7, v[86:87]
	v_cvt_pk_bf16_f32 v80, v74, v75
	v_lshl_add_u64 v[74:75], v[154:155], 0, v[76:77]
	global_store_dwordx4 v[74:75], v[78:81], off
	s_and_saveexec_b64 s[34:35], s[30:31]
	s_xor_b64 s[30:31], exec, s[34:35]
	s_or_saveexec_b64 s[30:31], s[30:31]
	v_add_u32_e32 v78, 0xb0, v158
	v_lshlrev_b32_e32 v74, 7, v78
	v_and_b32_e32 v74, 0xfff80, v74
	s_xor_b64 exec, exec, s[30:31]
	s_cbranch_execz .LBB0_158
	s_waitcnt vmcnt(1)
	v_pk_mul_f32 v[80:81], v[70:71], v[192:193] op_sel:[1,0] op_sel_hi:[0,0]
	v_pk_fma_f32 v[102:103], v[70:71], v[188:189], v[80:81] neg_lo:[0,0,1] neg_hi:[0,0,1]
	v_pk_fma_f32 v[70:71], v[70:71], v[188:189], v[80:81] op_sel_hi:[1,0,1]
	v_pk_mul_f32 v[80:81], v[72:73], v[192:193] op_sel:[1,1] op_sel_hi:[0,1]
	v_pk_fma_f32 v[192:193], v[72:73], v[188:189], v[80:81] op_sel:[0,1,0] neg_lo:[0,0,1] neg_hi:[0,0,1]
	v_pk_fma_f32 v[72:73], v[72:73], v[188:189], v[80:81] op_sel:[0,1,0]
	v_pk_mul_f32 v[80:81], v[66:67], v[194:195] op_sel:[1,0] op_sel_hi:[0,0]
	v_pk_fma_f32 v[188:189], v[66:67], v[190:191], v[80:81] neg_lo:[0,0,1] neg_hi:[0,0,1]
	v_pk_fma_f32 v[66:67], v[66:67], v[190:191], v[80:81] op_sel_hi:[1,0,1]
	v_mov_b32_e32 v80, v191
	v_mov_b32_e32 v189, v67
	v_pk_mul_f32 v[66:67], v[156:157], v[188:189] op_sel_hi:[0,1]
	v_mov_b32_e32 v188, v195
	v_pk_mul_f32 v[188:189], v[68:69], v[188:189] op_sel:[1,0] op_sel_hi:[0,0]
	v_pk_fma_f32 v[190:191], v[68:69], v[80:81], v[188:189] op_sel_hi:[1,0,1] neg_lo:[0,0,1] neg_hi:[0,0,1]
	v_pk_fma_f32 v[68:69], v[68:69], v[80:81], v[188:189] op_sel_hi:[1,0,1]
	v_mov_b32_e32 v103, v71
	v_mov_b32_e32 v193, v73
	v_mov_b32_e32 v191, v69
	v_pk_mul_f32 v[70:71], v[156:157], v[102:103] op_sel_hi:[0,1]
	v_pk_mul_f32 v[72:73], v[156:157], v[192:193] op_sel_hi:[0,1]
	v_pk_mul_f32 v[68:69], v[156:157], v[190:191] op_sel_hi:[0,1]

.LBB0_178:
	s_or_b64 exec, exec, s[34:35]
	s_xor_b64 s[30:31], s[30:31], -1
	s_and_saveexec_b64 s[34:35], s[30:31]
	s_xor_b64 s[34:35], exec, s[34:35]
	s_andn2_saveexec_b64 s[34:35], s[34:35]
	s_cbranch_execz .LBB0_182
	v_mov_b32_e32 v200, v158
	v_lshlrev_b32_e32 v200, 7, v200
	v_and_b32_e32 v200, 0xfff80, v200
	v_mov_b32_e32 v201, v141
	v_mov_b32_e32 v151, v141
	v_lshl_add_u64 v[196:197], s[10:11], 0, v[200:201]
	v_lshl_add_u64 v[198:199], s[12:13], 0, v[200:201]
	v_lshl_add_u64 v[196:197], v[196:197], 0, v[150:151]
	v_lshl_add_u64 v[198:199], v[198:199], 0, v[150:151]
	global_load_dwordx4 v[180:183], v[196:197], off
	global_load_dwordx4 v[184:187], v[198:199], off
	v_add_u32_e32 v200, 0x10, v158
	v_lshlrev_b32_e32 v200, 7, v200
	v_and_b32_e32 v200, 0xfff80, v200
	v_mov_b32_e32 v201, v141
	v_mov_b32_e32 v151, v141
	v_lshl_add_u64 v[196:197], s[10:11], 0, v[200:201]
	v_lshl_add_u64 v[198:199], s[12:13], 0, v[200:201]
	v_lshl_add_u64 v[196:197], v[196:197], 0, v[150:151]
	v_lshl_add_u64 v[198:199], v[198:199], 0, v[150:151]
	global_load_dwordx4 v[188:191], v[196:197], off
	global_load_dwordx4 v[192:195], v[198:199], off
	s_waitcnt vmcnt(2)
	v_pk_mul_f32 v[72:73], v[62:63], v[184:185] op_sel:[1,0] op_sel_hi:[0,0]
	v_pk_fma_f32 v[94:95], v[62:63], v[180:181], v[72:73] neg_lo:[0,0,1] neg_hi:[0,0,1]
	v_pk_fma_f32 v[62:63], v[62:63], v[180:181], v[72:73] op_sel_hi:[1,0,1]
	v_pk_mul_f32 v[72:73], v[64:65], v[184:185] op_sel:[1,1] op_sel_hi:[0,1]
	v_pk_fma_f32 v[184:185], v[64:65], v[180:181], v[72:73] op_sel:[0,1,0] neg_lo:[0,0,1] neg_hi:[0,0,1]
	v_pk_fma_f32 v[64:65], v[64:65], v[180:181], v[72:73] op_sel:[0,1,0]
	v_pk_mul_f32 v[72:73], v[58:59], v[186:187] op_sel:[1,0] op_sel_hi:[0,0]
	v_pk_fma_f32 v[180:181], v[58:59], v[182:183], v[72:73] neg_lo:[0,0,1] neg_hi:[0,0,1]
	v_pk_fma_f32 v[58:59], v[58:59], v[182:183], v[72:73] op_sel_hi:[1,0,1]
	v_mov_b32_e32 v72, v183
	v_mov_b32_e32 v181, v59
	v_pk_mul_f32 v[58:59], v[70:71], v[180:181] op_sel_hi:[0,1]
	v_mov_b32_e32 v180, v187
	v_pk_mul_f32 v[180:181], v[60:61], v[180:181] op_sel:[1,0] op_sel_hi:[0,0]
	v_pk_fma_f32 v[182:183], v[60:61], v[72:73], v[180:181] op_sel_hi:[1,0,1] neg_lo:[0,0,1] neg_hi:[0,0,1]
	v_pk_fma_f32 v[60:61], v[60:61], v[72:73], v[180:181] op_sel_hi:[1,0,1]
	v_mov_b32_e32 v95, v63
	v_mov_b32_e32 v185, v65
	v_mov_b32_e32 v183, v61
	v_pk_mul_f32 v[62:63], v[70:71], v[94:95] op_sel_hi:[0,1]
	v_pk_mul_f32 v[64:65], v[70:71], v[184:185] op_sel_hi:[0,1]
	v_pk_mul_f32 v[60:61], v[70:71], v[182:183] op_sel_hi:[0,1]
.LBB0_182:
	s_or_b64 exec, exec, s[34:35]
	v_cvt_pk_bf16_f32 v62, v62, v63
	v_cvt_pk_bf16_f32 v63, v64, v65
	v_cvt_pk_bf16_f32 v64, v58, v59
	v_cvt_pk_bf16_f32 v65, v60, v61
	v_lshl_add_u64 v[58:59], v[68:69], 0, v[124:125]
	global_store_dwordx4 v[58:59], v[62:65], off
	s_and_saveexec_b64 s[34:35], s[30:31]
	s_xor_b64 s[34:35], exec, s[34:35]
	s_andn2_saveexec_b64 s[34:35], s[34:35]
	s_cbranch_execz .LBB0_186
	v_add_u32_e32 v200, 0x20, v158
	v_lshlrev_b32_e32 v200, 7, v200
	v_and_b32_e32 v200, 0xfff80, v200
	v_mov_b32_e32 v201, v141
	v_mov_b32_e32 v151, v141
	v_lshl_add_u64 v[196:197], s[10:11], 0, v[200:201]
	v_lshl_add_u64 v[198:199], s[12:13], 0, v[200:201]
	v_lshl_add_u64 v[196:197], v[196:197], 0, v[150:151]
	v_lshl_add_u64 v[198:199], v[198:199], 0, v[150:151]
	global_load_dwordx4 v[180:183], v[196:197], off
	global_load_dwordx4 v[184:187], v[198:199], off
	s_waitcnt vmcnt(3)
	v_pk_mul_f32 v[72:73], v[54:55], v[192:193] op_sel:[1,0] op_sel_hi:[0,0]
	v_pk_mul_f32 v[192:193], v[56:57], v[192:193] op_sel:[1,1] op_sel_hi:[0,1]
	v_pk_fma_f32 v[78:79], v[54:55], v[188:189], v[72:73] neg_lo:[0,0,1] neg_hi:[0,0,1]
	v_pk_fma_f32 v[54:55], v[54:55], v[188:189], v[72:73] op_sel_hi:[1,0,1]
	v_pk_fma_f32 v[72:73], v[56:57], v[188:189], v[192:193] op_sel:[0,1,0] neg_lo:[0,0,1] neg_hi:[0,0,1]
	v_pk_fma_f32 v[56:57], v[56:57], v[188:189], v[192:193] op_sel:[0,1,0]
	v_pk_mul_f32 v[188:189], v[50:51], v[194:195] op_sel:[1,0] op_sel_hi:[0,0]
	v_pk_fma_f32 v[192:193], v[50:51], v[190:191], v[188:189] neg_lo:[0,0,1] neg_hi:[0,0,1]
	v_pk_fma_f32 v[50:51], v[50:51], v[190:191], v[188:189] op_sel_hi:[1,0,1]
	v_mov_b32_e32 v190, v195
	v_mov_b32_e32 v193, v51
	v_mov_b32_e32 v188, v191
	v_pk_mul_f32 v[190:191], v[52:53], v[190:191] op_sel:[1,0] op_sel_hi:[0,0]
	v_pk_mul_f32 v[50:51], v[70:71], v[192:193] op_sel_hi:[0,1]
	v_pk_fma_f32 v[192:193], v[52:53], v[188:189], v[190:191] op_sel_hi:[1,0,1] neg_lo:[0,0,1] neg_hi:[0,0,1]
	v_pk_fma_f32 v[52:53], v[52:53], v[188:189], v[190:191] op_sel_hi:[1,0,1]
	v_mov_b32_e32 v79, v55
	v_mov_b32_e32 v73, v57
	v_mov_b32_e32 v193, v53
	v_pk_mul_f32 v[54:55], v[70:71], v[78:79] op_sel_hi:[0,1]
	v_pk_mul_f32 v[56:57], v[70:71], v[72:73] op_sel_hi:[0,1]
	v_pk_mul_f32 v[52:53], v[70:71], v[192:193] op_sel_hi:[0,1]
.LBB0_186:
	s_or_b64 exec, exec, s[34:35]
	v_cvt_pk_bf16_f32 v54, v54, v55
	v_cvt_pk_bf16_f32 v55, v56, v57
	v_cvt_pk_bf16_f32 v56, v50, v51
	v_cvt_pk_bf16_f32 v57, v52, v53
	v_lshl_add_u64 v[50:51], v[68:69], 0, v[116:117]
	global_store_dwordx4 v[50:51], v[54:57], off
	s_and_saveexec_b64 s[34:35], s[30:31]
	s_xor_b64 s[34:35], exec, s[34:35]
	s_andn2_saveexec_b64 s[34:35], s[34:35]
	s_cbranch_execz .LBB0_190
	v_add_u32_e32 v200, 0x30, v158
	v_lshlrev_b32_e32 v200, 7, v200
	v_and_b32_e32 v200, 0xfff80, v200
	v_mov_b32_e32 v201, v141
	v_mov_b32_e32 v151, v141
	v_lshl_add_u64 v[196:197], s[10:11], 0, v[200:201]
	v_lshl_add_u64 v[198:199], s[12:13], 0, v[200:201]
	v_lshl_add_u64 v[196:197], v[196:197], 0, v[150:151]
	v_lshl_add_u64 v[198:199], v[198:199], 0, v[150:151]
	global_load_dwordx4 v[188:191], v[196:197], off
	global_load_dwordx4 v[192:195], v[198:199], off
	s_waitcnt vmcnt(3)
	v_pk_mul_f32 v[58:59], v[46:47], v[184:185] op_sel:[1,0] op_sel_hi:[0,0]
	v_pk_mul_f32 v[184:185], v[48:49], v[184:185] op_sel:[1,1] op_sel_hi:[0,1]
	v_pk_fma_f32 v[60:61], v[46:47], v[180:181], v[58:59] neg_lo:[0,0,1] neg_hi:[0,0,1]
	v_pk_fma_f32 v[46:47], v[46:47], v[180:181], v[58:59] op_sel_hi:[1,0,1]
	v_pk_fma_f32 v[58:59], v[48:49], v[180:181], v[184:185] op_sel:[0,1,0] neg_lo:[0,0,1] neg_hi:[0,0,1]
	v_pk_fma_f32 v[48:49], v[48:49], v[180:181], v[184:185] op_sel:[0,1,0]
	v_pk_mul_f32 v[180:181], v[42:43], v[186:187] op_sel:[1,0] op_sel_hi:[0,0]
	v_pk_fma_f32 v[184:185], v[42:43], v[182:183], v[180:181] neg_lo:[0,0,1] neg_hi:[0,0,1]
	v_pk_fma_f32 v[42:43], v[42:43], v[182:183], v[180:181] op_sel_hi:[1,0,1]
	v_mov_b32_e32 v182, v187
	v_mov_b32_e32 v185, v43
	v_mov_b32_e32 v180, v183
	v_pk_mul_f32 v[182:183], v[44:45], v[182:183] op_sel:[1,0] op_sel_hi:[0,0]
	v_pk_mul_f32 v[42:43], v[70:71], v[184:185] op_sel_hi:[0,1]
	v_pk_fma_f32 v[184:185], v[44:45], v[180:181], v[182:183] op_sel_hi:[1,0,1] neg_lo:[0,0,1] neg_hi:[0,0,1]
	v_pk_fma_f32 v[44:45], v[44:45], v[180:181], v[182:183] op_sel_hi:[1,0,1]
	v_mov_b32_e32 v61, v47
	v_mov_b32_e32 v59, v49
	v_mov_b32_e32 v185, v45
	v_pk_mul_f32 v[46:47], v[70:71], v[60:61] op_sel_hi:[0,1]
	v_pk_mul_f32 v[48:49], v[70:71], v[58:59] op_sel_hi:[0,1]
	v_pk_mul_f32 v[44:45], v[70:71], v[184:185] op_sel_hi:[0,1]
.LBB0_190:
	s_or_b64 exec, exec, s[34:35]
	v_cvt_pk_bf16_f32 v46, v46, v47
	v_cvt_pk_bf16_f32 v47, v48, v49
	v_cvt_pk_bf16_f32 v48, v42, v43
	v_cvt_pk_bf16_f32 v49, v44, v45
	v_lshl_add_u64 v[42:43], v[68:69], 0, v[108:109]
	global_store_dwordx4 v[42:43], v[46:49], off
	s_and_saveexec_b64 s[34:35], s[30:31]
	s_xor_b64 s[34:35], exec, s[34:35]
	s_andn2_saveexec_b64 s[34:35], s[34:35]
	s_cbranch_execz .LBB0_194
	v_add_u32_e32 v200, 0x80, v158
	v_lshlrev_b32_e32 v200, 7, v200
	v_and_b32_e32 v200, 0xfff80, v200
	v_mov_b32_e32 v201, v141
	v_mov_b32_e32 v151, v141
	v_lshl_add_u64 v[196:197], s[10:11], 0, v[200:201]
	v_lshl_add_u64 v[198:199], s[12:13], 0, v[200:201]
	v_lshl_add_u64 v[196:197], v[196:197], 0, v[150:151]
	v_lshl_add_u64 v[198:199], v[198:199], 0, v[150:151]
	global_load_dwordx4 v[180:183], v[196:197], off
	global_load_dwordx4 v[184:187], v[198:199], off
	s_waitcnt vmcnt(3)
	v_pk_mul_f32 v[50:51], v[38:39], v[192:193] op_sel:[1,0] op_sel_hi:[0,0]
	v_pk_mul_f32 v[192:193], v[40:41], v[192:193] op_sel:[1,1] op_sel_hi:[0,1]
	v_pk_fma_f32 v[52:53], v[38:39], v[188:189], v[50:51] neg_lo:[0,0,1] neg_hi:[0,0,1]
	v_pk_fma_f32 v[38:39], v[38:39], v[188:189], v[50:51] op_sel_hi:[1,0,1]
	v_pk_fma_f32 v[50:51], v[40:41], v[188:189], v[192:193] op_sel:[0,1,0] neg_lo:[0,0,1] neg_hi:[0,0,1]
	v_pk_fma_f32 v[40:41], v[40:41], v[188:189], v[192:193] op_sel:[0,1,0]
	v_pk_mul_f32 v[188:189], v[34:35], v[194:195] op_sel:[1,0] op_sel_hi:[0,0]
	v_pk_fma_f32 v[192:193], v[34:35], v[190:191], v[188:189] neg_lo:[0,0,1] neg_hi:[0,0,1]
	v_pk_fma_f32 v[34:35], v[34:35], v[190:191], v[188:189] op_sel_hi:[1,0,1]
	v_mov_b32_e32 v190, v195
	v_mov_b32_e32 v193, v35
	v_mov_b32_e32 v188, v191
	v_pk_mul_f32 v[190:191], v[36:37], v[190:191] op_sel:[1,0] op_sel_hi:[0,0]
	v_pk_mul_f32 v[34:35], v[70:71], v[192:193] op_sel_hi:[0,1]
	v_pk_fma_f32 v[192:193], v[36:37], v[188:189], v[190:191] op_sel_hi:[1,0,1] neg_lo:[0,0,1] neg_hi:[0,0,1]
	v_pk_fma_f32 v[36:37], v[36:37], v[188:189], v[190:191] op_sel_hi:[1,0,1]
	v_mov_b32_e32 v53, v39
	v_mov_b32_e32 v51, v41
	v_mov_b32_e32 v193, v37
	v_pk_mul_f32 v[38:39], v[70:71], v[52:53] op_sel_hi:[0,1]
	v_pk_mul_f32 v[40:41], v[70:71], v[50:51] op_sel_hi:[0,1]
	v_pk_mul_f32 v[36:37], v[70:71], v[192:193] op_sel_hi:[0,1]
.LBB0_194:
	s_or_b64 exec, exec, s[34:35]
	v_cvt_pk_bf16_f32 v38, v38, v39
	v_cvt_pk_bf16_f32 v39, v40, v41
	v_cvt_pk_bf16_f32 v40, v34, v35
	v_cvt_pk_bf16_f32 v41, v36, v37
	v_lshl_add_u64 v[34:35], v[68:69], 0, v[100:101]
	global_store_dwordx4 v[34:35], v[38:41], off
	s_and_saveexec_b64 s[34:35], s[30:31]
	s_xor_b64 s[34:35], exec, s[34:35]
	s_andn2_saveexec_b64 s[34:35], s[34:35]
	s_cbranch_execz .LBB0_198
	v_add_u32_e32 v200, 0x90, v158
	v_lshlrev_b32_e32 v200, 7, v200
	v_and_b32_e32 v200, 0xfff80, v200
	v_mov_b32_e32 v201, v141
	v_mov_b32_e32 v151, v141
	v_lshl_add_u64 v[196:197], s[10:11], 0, v[200:201]
	v_lshl_add_u64 v[198:199], s[12:13], 0, v[200:201]
	v_lshl_add_u64 v[196:197], v[196:197], 0, v[150:151]
	v_lshl_add_u64 v[198:199], v[198:199], 0, v[150:151]
	global_load_dwordx4 v[188:191], v[196:197], off
	global_load_dwordx4 v[192:195], v[198:199], off
	s_waitcnt vmcnt(3)
	v_pk_mul_f32 v[42:43], v[30:31], v[184:185] op_sel:[1,0] op_sel_hi:[0,0]
	v_pk_mul_f32 v[184:185], v[32:33], v[184:185] op_sel:[1,1] op_sel_hi:[0,1]
	v_pk_fma_f32 v[44:45], v[30:31], v[180:181], v[42:43] neg_lo:[0,0,1] neg_hi:[0,0,1]
	v_pk_fma_f32 v[30:31], v[30:31], v[180:181], v[42:43] op_sel_hi:[1,0,1]
	v_pk_fma_f32 v[42:43], v[32:33], v[180:181], v[184:185] op_sel:[0,1,0] neg_lo:[0,0,1] neg_hi:[0,0,1]
	v_pk_fma_f32 v[32:33], v[32:33], v[180:181], v[184:185] op_sel:[0,1,0]
	v_pk_mul_f32 v[180:181], v[26:27], v[186:187] op_sel:[1,0] op_sel_hi:[0,0]
	v_pk_fma_f32 v[184:185], v[26:27], v[182:183], v[180:181] neg_lo:[0,0,1] neg_hi:[0,0,1]
	v_pk_fma_f32 v[26:27], v[26:27], v[182:183], v[180:181] op_sel_hi:[1,0,1]
	v_mov_b32_e32 v182, v187
	v_mov_b32_e32 v185, v27
	v_mov_b32_e32 v180, v183
	v_pk_mul_f32 v[182:183], v[28:29], v[182:183] op_sel:[1,0] op_sel_hi:[0,0]
	v_pk_mul_f32 v[26:27], v[70:71], v[184:185] op_sel_hi:[0,1]
	v_pk_fma_f32 v[184:185], v[28:29], v[180:181], v[182:183] op_sel_hi:[1,0,1] neg_lo:[0,0,1] neg_hi:[0,0,1]
	v_pk_fma_f32 v[28:29], v[28:29], v[180:181], v[182:183] op_sel_hi:[1,0,1]
	v_mov_b32_e32 v45, v31
	v_mov_b32_e32 v43, v33
	v_mov_b32_e32 v185, v29
	v_pk_mul_f32 v[30:31], v[70:71], v[44:45] op_sel_hi:[0,1]
	v_pk_mul_f32 v[32:33], v[70:71], v[42:43] op_sel_hi:[0,1]
	v_pk_mul_f32 v[28:29], v[70:71], v[184:185] op_sel_hi:[0,1]
.LBB0_198:
	s_or_b64 exec, exec, s[34:35]
	v_cvt_pk_bf16_f32 v30, v30, v31
	v_cvt_pk_bf16_f32 v31, v32, v33
	v_cvt_pk_bf16_f32 v32, v26, v27
	v_cvt_pk_bf16_f32 v33, v28, v29
	v_lshl_add_u64 v[26:27], v[68:69], 0, v[92:93]
	global_store_dwordx4 v[26:27], v[30:33], off
	s_and_saveexec_b64 s[34:35], s[30:31]
	s_xor_b64 s[34:35], exec, s[34:35]
	s_andn2_saveexec_b64 s[34:35], s[34:35]
	s_cbranch_execz .LBB0_202
	v_add_u32_e32 v200, 0xa0, v158
	v_lshlrev_b32_e32 v200, 7, v200
	v_and_b32_e32 v200, 0xfff80, v200
	v_mov_b32_e32 v201, v141
	v_mov_b32_e32 v151, v141
	v_lshl_add_u64 v[196:197], s[10:11], 0, v[200:201]
	v_lshl_add_u64 v[198:199], s[12:13], 0, v[200:201]
	v_lshl_add_u64 v[196:197], v[196:197], 0, v[150:151]
	v_lshl_add_u64 v[198:199], v[198:199], 0, v[150:151]
	global_load_dwordx4 v[180:183], v[196:197], off
	global_load_dwordx4 v[184:187], v[198:199], off
	s_waitcnt vmcnt(3)
	v_pk_mul_f32 v[34:35], v[22:23], v[192:193] op_sel:[1,0] op_sel_hi:[0,0]
	v_pk_mul_f32 v[192:193], v[24:25], v[192:193] op_sel:[1,1] op_sel_hi:[0,1]
	v_pk_fma_f32 v[36:37], v[22:23], v[188:189], v[34:35] neg_lo:[0,0,1] neg_hi:[0,0,1]
	v_pk_fma_f32 v[22:23], v[22:23], v[188:189], v[34:35] op_sel_hi:[1,0,1]
	v_pk_fma_f32 v[34:35], v[24:25], v[188:189], v[192:193] op_sel:[0,1,0] neg_lo:[0,0,1] neg_hi:[0,0,1]
	v_pk_fma_f32 v[24:25], v[24:25], v[188:189], v[192:193] op_sel:[0,1,0]
	v_pk_mul_f32 v[188:189], v[18:19], v[194:195] op_sel:[1,0] op_sel_hi:[0,0]
	v_pk_fma_f32 v[192:193], v[18:19], v[190:191], v[188:189] neg_lo:[0,0,1] neg_hi:[0,0,1]
	v_pk_fma_f32 v[18:19], v[18:19], v[190:191], v[188:189] op_sel_hi:[1,0,1]
	v_mov_b32_e32 v190, v195
	v_mov_b32_e32 v193, v19
	v_mov_b32_e32 v188, v191
	v_pk_mul_f32 v[190:191], v[20:21], v[190:191] op_sel:[1,0] op_sel_hi:[0,0]
	v_pk_mul_f32 v[18:19], v[70:71], v[192:193] op_sel_hi:[0,1]
	v_pk_fma_f32 v[192:193], v[20:21], v[188:189], v[190:191] op_sel_hi:[1,0,1] neg_lo:[0,0,1] neg_hi:[0,0,1]
	v_pk_fma_f32 v[20:21], v[20:21], v[188:189], v[190:191] op_sel_hi:[1,0,1]
	v_mov_b32_e32 v37, v23
	v_mov_b32_e32 v35, v25
	v_mov_b32_e32 v193, v21
	v_pk_mul_f32 v[22:23], v[70:71], v[36:37] op_sel_hi:[0,1]
	v_pk_mul_f32 v[24:25], v[70:71], v[34:35] op_sel_hi:[0,1]
	v_pk_mul_f32 v[20:21], v[70:71], v[192:193] op_sel_hi:[0,1]
.LBB0_202:
	s_or_b64 exec, exec, s[34:35]
	v_cvt_pk_bf16_f32 v22, v22, v23
	v_cvt_pk_bf16_f32 v23, v24, v25
	v_cvt_pk_bf16_f32 v24, v18, v19
	v_cvt_pk_bf16_f32 v25, v20, v21
	v_lshl_add_u64 v[18:19], v[68:69], 0, v[84:85]
	global_store_dwordx4 v[18:19], v[22:25], off
	s_and_saveexec_b64 s[34:35], s[30:31]
	s_xor_b64 s[34:35], exec, s[34:35]
	s_andn2_saveexec_b64 s[34:35], s[34:35]
	s_cbranch_execz .LBB0_206
	v_add_u32_e32 v200, 0xb0, v158
	v_lshlrev_b32_e32 v200, 7, v200
	v_and_b32_e32 v200, 0xfff80, v200
	v_mov_b32_e32 v201, v141
	v_mov_b32_e32 v151, v141
	v_lshl_add_u64 v[196:197], s[10:11], 0, v[200:201]
	v_lshl_add_u64 v[198:199], s[12:13], 0, v[200:201]
	v_lshl_add_u64 v[196:197], v[196:197], 0, v[150:151]
	v_lshl_add_u64 v[198:199], v[198:199], 0, v[150:151]
	global_load_dwordx4 v[188:191], v[196:197], off
	global_load_dwordx4 v[192:195], v[198:199], off
	s_waitcnt vmcnt(3)
	v_pk_mul_f32 v[26:27], v[14:15], v[184:185] op_sel:[1,0] op_sel_hi:[0,0]
	v_pk_mul_f32 v[184:185], v[16:17], v[184:185] op_sel:[1,1] op_sel_hi:[0,1]
	v_pk_fma_f32 v[28:29], v[14:15], v[180:181], v[26:27] neg_lo:[0,0,1] neg_hi:[0,0,1]
	v_pk_fma_f32 v[14:15], v[14:15], v[180:181], v[26:27] op_sel_hi:[1,0,1]
	v_pk_fma_f32 v[26:27], v[16:17], v[180:181], v[184:185] op_sel:[0,1,0] neg_lo:[0,0,1] neg_hi:[0,0,1]
	v_pk_fma_f32 v[16:17], v[16:17], v[180:181], v[184:185] op_sel:[0,1,0]
	v_pk_mul_f32 v[180:181], v[10:11], v[186:187] op_sel:[1,0] op_sel_hi:[0,0]
	v_pk_fma_f32 v[184:185], v[10:11], v[182:183], v[180:181] neg_lo:[0,0,1] neg_hi:[0,0,1]
	v_pk_fma_f32 v[10:11], v[10:11], v[182:183], v[180:181] op_sel_hi:[1,0,1]
	v_mov_b32_e32 v182, v187
	v_mov_b32_e32 v185, v11
	v_mov_b32_e32 v180, v183
	v_pk_mul_f32 v[182:183], v[12:13], v[182:183] op_sel:[1,0] op_sel_hi:[0,0]
	v_pk_mul_f32 v[10:11], v[70:71], v[184:185] op_sel_hi:[0,1]
	v_pk_fma_f32 v[184:185], v[12:13], v[180:181], v[182:183] op_sel_hi:[1,0,1] neg_lo:[0,0,1] neg_hi:[0,0,1]
	v_pk_fma_f32 v[12:13], v[12:13], v[180:181], v[182:183] op_sel_hi:[1,0,1]
	v_mov_b32_e32 v29, v15
	v_mov_b32_e32 v27, v17
	v_mov_b32_e32 v185, v13
	v_pk_mul_f32 v[14:15], v[70:71], v[28:29] op_sel_hi:[0,1]
	v_pk_mul_f32 v[16:17], v[70:71], v[26:27] op_sel_hi:[0,1]
	v_pk_mul_f32 v[12:13], v[70:71], v[184:185] op_sel_hi:[0,1]
.LBB0_206:
	s_or_b64 exec, exec, s[34:35]
	v_cvt_pk_bf16_f32 v14, v14, v15
	v_cvt_pk_bf16_f32 v15, v16, v17
	v_cvt_pk_bf16_f32 v16, v10, v11
	v_cvt_pk_bf16_f32 v17, v12, v13
	v_lshl_add_u64 v[10:11], v[68:69], 0, v[76:77]
	global_store_dwordx4 v[10:11], v[14:17], off
	s_and_saveexec_b64 s[34:35], s[30:31]
	s_xor_b64 s[30:31], exec, s[34:35]
	s_andn2_saveexec_b64 s[30:31], s[30:31]
	s_cbranch_execz .LBB0_110
	s_waitcnt vmcnt(1)
	v_pk_mul_f32 v[18:19], v[6:7], v[192:193] op_sel:[1,0] op_sel_hi:[0,0]
	v_pk_mul_f32 v[192:193], v[8:9], v[192:193] op_sel:[1,1] op_sel_hi:[0,1]
	v_pk_fma_f32 v[20:21], v[6:7], v[188:189], v[18:19] neg_lo:[0,0,1] neg_hi:[0,0,1]
	v_pk_fma_f32 v[6:7], v[6:7], v[188:189], v[18:19] op_sel_hi:[1,0,1]
	v_pk_fma_f32 v[18:19], v[8:9], v[188:189], v[192:193] op_sel:[0,1,0] neg_lo:[0,0,1] neg_hi:[0,0,1]
	v_pk_fma_f32 v[8:9], v[8:9], v[188:189], v[192:193] op_sel:[0,1,0]
	v_pk_mul_f32 v[188:189], v[2:3], v[194:195] op_sel:[1,0] op_sel_hi:[0,0]
	v_pk_fma_f32 v[192:193], v[2:3], v[190:191], v[188:189] neg_lo:[0,0,1] neg_hi:[0,0,1]
	v_pk_fma_f32 v[2:3], v[2:3], v[190:191], v[188:189] op_sel_hi:[1,0,1]
	v_mov_b32_e32 v190, v195
	v_mov_b32_e32 v193, v3
	v_mov_b32_e32 v188, v191
	v_pk_mul_f32 v[190:191], v[4:5], v[190:191] op_sel:[1,0] op_sel_hi:[0,0]
	v_pk_mul_f32 v[2:3], v[70:71], v[192:193] op_sel_hi:[0,1]
	v_pk_fma_f32 v[192:193], v[4:5], v[188:189], v[190:191] op_sel_hi:[1,0,1] neg_lo:[0,0,1] neg_hi:[0,0,1]
	v_pk_fma_f32 v[4:5], v[4:5], v[188:189], v[190:191] op_sel_hi:[1,0,1]
	v_mov_b32_e32 v21, v7
	v_mov_b32_e32 v19, v9
	v_mov_b32_e32 v193, v5
	v_pk_mul_f32 v[6:7], v[70:71], v[20:21] op_sel_hi:[0,1]
	v_pk_mul_f32 v[8:9], v[70:71], v[18:19] op_sel_hi:[0,1]
	v_pk_mul_f32 v[4:5], v[70:71], v[192:193] op_sel_hi:[0,1]
	s_branch .LBB0_110
